# baseline (speedup 1.0000x reference)
.LBB1_3:
	s_mov_b32 s29, s16
	v_add_u32_e32 v0, s29, v101
	ds_read_b128 v[94:97], v0 offset:16384
	ds_read_b128 v[102:105], v0 offset:17408
	ds_read_b128 v[106:109], v0 offset:18432
	ds_read_b128 v[110:113], v0 offset:19456
	ds_read_b128 v[114:117], v0 offset:32768
	ds_read_b128 v[118:121], v0 offset:33792
	ds_read_b128 v[122:125], v0 offset:34816
	ds_read_b128 v[126:129], v0 offset:35840
	v_add_u32_e32 v0, s29, v91
	ds_read_b128 v[130:133], v0
	ds_read_b128 v[134:137], v0 offset:1024
	ds_read_b128 v[138:141], v0 offset:2048
	ds_read_b128 v[142:145], v0 offset:3072
	ds_read_b128 v[146:149], v0 offset:4096
	ds_read_b128 v[150:153], v0 offset:5120
	ds_read_b128 v[154:157], v0 offset:6144
	ds_read_b128 v[158:161], v0 offset:7168
	s_lshl_b32 s16, s28, 2
	s_or_b32 s16, s16, s23
	s_lshl_b64 s[30:31], s[16:17], 19
	s_add_u32 s16, s6, s30
	s_addc_u32 s31, s7, s31
	s_lshl_b32 s33, s3, 7
	s_ashr_i32 s35, s33, 31
	s_add_u32 s30, s16, s33
	s_addc_u32 s31, s31, s35
	s_add_u32 s34, s4, s33
	s_addc_u32 s35, s5, s35
	s_add_i32 s16, s19, s27
	s_add_i32 m0, s16, 0x4000
	s_nop 0
	global_load_lds_dwordx4 v84, s[30:31]
	s_add_i32 m0, s16, 0x6000
	s_nop 0
	global_load_lds_dwordx4 v88, s[30:31]
	s_mov_b32 m0, s16
	s_nop 0
	global_load_lds_dwordx4 v82, s[34:35]
	s_waitcnt vmcnt(3)
	s_waitcnt lgkmcnt(0)
	s_barrier
	s_setprio 1
	s_waitcnt lgkmcnt(0)
	v_mfma_f32_16x16x32_f16 v[78:81], v[94:97], v[130:133], v[78:81]
	s_add_u32 s30, s30, 0x40000
	s_addc_u32 s31, s31, 0
	s_add_i32 m0, s16, 0x8000
	v_mfma_f32_16x16x32_f16 v[74:77], v[106:109], v[130:133], v[74:77]
	global_load_lds_dwordx4 v84, s[30:31]
	s_add_i32 m0, s16, 0xa000
	v_mfma_f32_16x16x32_f16 v[66:69], v[94:97], v[138:141], v[66:69]
	global_load_lds_dwordx4 v88, s[30:31]
	s_add_i32 m0, s16, 0x2000
	v_mfma_f32_16x16x32_f16 v[58:61], v[106:109], v[138:141], v[58:61]
	global_load_lds_dwordx4 v86, s[34:35]
	v_mfma_f32_16x16x32_f16 v[78:81], v[102:105], v[134:137], v[78:81]
	v_mfma_f32_16x16x32_f16 v[74:77], v[110:113], v[134:137], v[74:77]
	v_mfma_f32_16x16x32_f16 v[66:69], v[102:105], v[142:145], v[66:69]
	v_mfma_f32_16x16x32_f16 v[58:61], v[110:113], v[142:145], v[58:61]
	v_mfma_f32_16x16x32_f16 v[54:57], v[94:97], v[146:149], v[54:57]
	v_mfma_f32_16x16x32_f16 v[46:49], v[106:109], v[146:149], v[46:49]
	v_mfma_f32_16x16x32_f16 v[34:37], v[94:97], v[154:157], v[34:37]
	v_mfma_f32_16x16x32_f16 v[26:29], v[106:109], v[154:157], v[26:29]
	v_mfma_f32_16x16x32_f16 v[54:57], v[102:105], v[150:153], v[54:57]
	v_mfma_f32_16x16x32_f16 v[46:49], v[110:113], v[150:153], v[46:49]
	v_mfma_f32_16x16x32_f16 v[34:37], v[102:105], v[158:161], v[34:37]
	v_mfma_f32_16x16x32_f16 v[26:29], v[110:113], v[158:161], v[26:29]
	v_mfma_f32_16x16x32_f16 v[70:73], v[114:117], v[130:133], v[70:73]
	v_mfma_f32_16x16x32_f16 v[62:65], v[122:125], v[130:133], v[62:65]
	v_mfma_f32_16x16x32_f16 v[50:53], v[114:117], v[138:141], v[50:53]
	v_mfma_f32_16x16x32_f16 v[42:45], v[122:125], v[138:141], v[42:45]
	v_mfma_f32_16x16x32_f16 v[70:73], v[118:121], v[134:137], v[70:73]
	v_mfma_f32_16x16x32_f16 v[62:65], v[126:129], v[134:137], v[62:65]
	v_mfma_f32_16x16x32_f16 v[50:53], v[118:121], v[142:145], v[50:53]
	v_mfma_f32_16x16x32_f16 v[42:45], v[126:129], v[142:145], v[42:45]
	v_mfma_f32_16x16x32_f16 v[38:41], v[114:117], v[146:149], v[38:41]
	v_mfma_f32_16x16x32_f16 v[30:33], v[122:125], v[146:149], v[30:33]
	s_add_i32 s3, s3, 1
	s_cmp_lt_u32 s28, 2
	s_cselect_b64 s[30:31], -1, 0
	v_mfma_f32_16x16x32_f16 v[22:25], v[114:117], v[154:157], v[22:25]
	s_cmp_eq_u32 s3, 16
	s_cselect_b64 s[34:35], -1, 0
	v_mfma_f32_16x16x32_f16 v[2:5], v[122:125], v[154:157], v[2:5]
	s_and_b64 s[36:37], s[34:35], exec
	s_cselect_b32 s3, 0, s3
	v_mfma_f32_16x16x32_f16 v[38:41], v[118:121], v[150:153], v[38:41]
	s_and_b64 s[30:31], s[34:35], s[30:31]
	s_cmp_lg_u64 s[30:31], 0
	v_mfma_f32_16x16x32_f16 v[30:33], v[126:129], v[150:153], v[30:33]
	s_addc_u32 s28, s28, 0
	s_add_i32 s26, s26, -1
	v_mfma_f32_16x16x32_f16 v[22:25], v[118:121], v[158:161], v[22:25]
	s_mov_b32 s16, s24
	s_mov_b32 s24, s27
	v_mfma_f32_16x16x32_f16 v[2:5], v[126:129], v[158:161], v[2:5]
	s_mov_b32 s27, s29
	s_cmp_lg_u32 s26, 0
	s_setprio 0
	s_barrier
	s_cbranch_scc1 .LBB1_3
	s_lshl_b32 s3, s14, 7
	s_add_i32 s17, s25, s3
	s_ashr_i32 s3, s17, 1
	s_lshr_b32 s14, s17, 5
	s_or_b32 s24, s15, s2
	s_and_b32 s14, s14, 62
	s_and_b32 s27, s3, 0xfffffc00
	v_or_b32_e32 v105, s24, v1
	v_lshlrev_b32_e32 v98, 4, v93
	v_or_b32_e32 v102, 16, v93
	v_or_b32_e32 v103, 32, v93
	v_or_b32_e32 v104, 48, v93
	v_mov_b32_e32 v93, 0
	s_and_b32 s16, s24, 0x340
	v_lshlrev_b32_e32 v95, 6, v105
	s_or_b32 s2, s27, s14
	v_lshlrev_b32_e32 v0, 9, v92
	v_and_b32_e32 v110, 0xc00, v95
	v_mov_b32_e32 v111, v93
	s_or_b32 s14, s2, s16
	v_and_b32_e32 v92, 0x200, v0
	v_lshl_add_u64 v[110:111], s[8:9], 0, v[110:111]
	s_or_b32 s30, s14, 0x80
	s_mov_b32 s3, 0
	v_mov_b32_e32 v99, v93
	v_lshl_add_u64 v[110:111], v[110:111], 0, v[92:93]
	s_mov_b32 s2, 0x3e38aa3b
	v_pk_add_f32 v[72:73], v[12:13], v[72:73]
	v_pk_add_f32 v[70:71], v[10:11], v[70:71]
	v_pk_add_f32 v[64:65], v[8:9], v[64:65]
	v_pk_add_f32 v[62:63], v[6:7], v[62:63]
	s_ashr_i32 s31, s30, 31
	v_lshl_add_u64 v[112:113], v[110:111], 0, v[98:99]
	v_pk_mul_f32 v[72:73], v[72:73], s[2:3] op_sel_hi:[1,0]
	v_pk_mul_f32 v[70:71], v[70:71], s[2:3] op_sel_hi:[1,0]
	v_pk_mul_f32 v[64:65], v[64:65], s[2:3] op_sel_hi:[1,0]
	v_pk_mul_f32 v[62:63], v[62:63], s[2:3] op_sel_hi:[1,0]
	s_lshl_b64 s[30:31], s[30:31], 12
	v_lshlrev_b32_e32 v96, 4, v102
	v_mov_b32_e32 v97, v93
	v_pk_add_f32 v[80:81], v[20:21], v[80:81]
	v_pk_add_f32 v[78:79], v[18:19], v[78:79]
	v_pk_add_f32 v[74:75], v[14:15], v[74:75]
	s_ashr_i32 s15, s14, 31
	v_cvt_pk_f16_f32 v70, v70, v71
	v_cvt_pk_f16_f32 v71, v72, v73
	v_cvt_pk_f16_f32 v72, v62, v63
	v_cvt_pk_f16_f32 v73, v64, v65
	v_lshl_add_u64 v[62:63], v[112:113], 0, s[30:31]
	v_pk_add_f32 v[58:59], v[14:15], v[58:59]
	v_pk_mul_f32 v[80:81], v[80:81], s[2:3] op_sel_hi:[1,0]
	v_pk_mul_f32 v[78:79], v[78:79], s[2:3] op_sel_hi:[1,0]
	v_pk_mul_f32 v[74:75], v[74:75], s[2:3] op_sel_hi:[1,0]
	s_lshl_b64 s[28:29], s[14:15], 12
	global_store_dwordx4 v[62:63], v[70:73], off sc1
	v_pk_add_f32 v[62:63], v[20:21], v[68:69]
	v_pk_add_f32 v[64:65], v[18:19], v[66:67]
	v_lshl_add_u64 v[70:71], v[110:111], 0, v[96:97]
	v_pk_mul_f32 v[58:59], v[58:59], s[2:3] op_sel_hi:[1,0]
	v_pk_add_f32 v[52:53], v[12:13], v[52:53]
	v_pk_add_f32 v[50:51], v[10:11], v[50:51]
	v_pk_add_f32 v[44:45], v[8:9], v[44:45]
	v_pk_add_f32 v[42:43], v[6:7], v[42:43]
	v_lshlrev_b32_e32 v0, 4, v103
	v_cvt_pk_f16_f32 v78, v78, v79
	v_cvt_pk_f16_f32 v79, v80, v81
	v_cvt_pk_f16_f32 v80, v74, v75
	v_lshl_add_u64 v[74:75], v[112:113], 0, s[28:29]
	v_pk_mul_f32 v[66:67], v[62:63], s[2:3] op_sel_hi:[1,0]
	v_pk_mul_f32 v[62:63], v[64:65], s[2:3] op_sel_hi:[1,0]
	v_cvt_pk_f16_f32 v64, v58, v59
	v_lshl_add_u64 v[58:59], v[70:71], 0, s[28:29]
	v_pk_mul_f32 v[52:53], v[52:53], s[2:3] op_sel_hi:[1,0]
	v_pk_mul_f32 v[50:51], v[50:51], s[2:3] op_sel_hi:[1,0]
	v_pk_mul_f32 v[44:45], v[44:45], s[2:3] op_sel_hi:[1,0]
	v_pk_mul_f32 v[42:43], v[42:43], s[2:3] op_sel_hi:[1,0]
	s_or_b32 s28, s14, 1
	s_or_b32 s14, s14, 0x81
	v_and_b32_e32 v106, 0xf0, v0
	v_mov_b32_e32 v107, v93
	v_cvt_pk_f16_f32 v50, v50, v51
	v_cvt_pk_f16_f32 v51, v52, v53
	v_cvt_pk_f16_f32 v52, v42, v43
	v_cvt_pk_f16_f32 v53, v44, v45
	v_lshl_add_u64 v[42:43], v[70:71], 0, s[30:31]
	v_pk_add_f32 v[40:41], v[12:13], v[40:41]
	v_pk_add_f32 v[38:39], v[10:11], v[38:39]
	v_pk_add_f32 v[32:33], v[8:9], v[32:33]
	v_pk_add_f32 v[30:31], v[6:7], v[30:31]
	s_ashr_i32 s15, s14, 31
	v_lshlrev_b32_e32 v94, 4, v104
	global_store_dwordx4 v[42:43], v[50:53], off sc1
	v_pk_mul_f32 v[40:41], v[40:41], s[2:3] op_sel_hi:[1,0]
	v_pk_mul_f32 v[38:39], v[38:39], s[2:3] op_sel_hi:[1,0]
	v_lshl_add_u64 v[50:51], v[110:111], 0, v[106:107]
	v_pk_mul_f32 v[32:33], v[32:33], s[2:3] op_sel_hi:[1,0]
	v_pk_mul_f32 v[30:31], v[30:31], s[2:3] op_sel_hi:[1,0]
	s_lshl_b64 s[14:15], s[14:15], 12
	v_and_b32_e32 v108, 0x1f0, v94
	v_mov_b32_e32 v109, v93
	v_pk_add_f32 v[42:43], v[20:21], v[56:57]
	v_pk_add_f32 v[44:45], v[18:19], v[54:55]
	v_pk_add_f32 v[46:47], v[14:15], v[46:47]
	s_ashr_i32 s29, s28, 31
	v_cvt_pk_f16_f32 v38, v38, v39
	v_cvt_pk_f16_f32 v39, v40, v41
	v_cvt_pk_f16_f32 v40, v30, v31
	v_cvt_pk_f16_f32 v41, v32, v33
	v_lshl_add_u64 v[30:31], v[50:51], 0, s[14:15]
	v_pk_add_f32 v[20:21], v[20:21], v[36:37]
	v_pk_add_f32 v[18:19], v[18:19], v[34:35]
	v_pk_add_f32 v[14:15], v[14:15], v[26:27]
	v_pk_add_f32 v[76:77], v[16:17], v[76:77]
	v_pk_add_f32 v[60:61], v[16:17], v[60:61]
	v_pk_mul_f32 v[52:53], v[42:43], s[2:3] op_sel_hi:[1,0]
	v_pk_mul_f32 v[42:43], v[44:45], s[2:3] op_sel_hi:[1,0]
	v_pk_add_f32 v[44:45], v[16:17], v[48:49]
	s_lshl_b64 s[28:29], s[28:29], 12
	global_store_dwordx4 v[30:31], v[38:41], off sc1
	v_lshl_add_u64 v[30:31], v[110:111], 0, v[108:109]
	v_pk_mul_f32 v[20:21], v[20:21], s[2:3] op_sel_hi:[1,0]
	v_pk_mul_f32 v[18:19], v[18:19], s[2:3] op_sel_hi:[1,0]
	v_pk_add_f32 v[16:17], v[16:17], v[28:29]
	v_pk_mul_f32 v[14:15], v[14:15], s[2:3] op_sel_hi:[1,0]
	v_pk_add_f32 v[12:13], v[12:13], v[24:25]
	v_pk_add_f32 v[10:11], v[10:11], v[22:23]
	v_pk_add_f32 v[4:5], v[8:9], v[4:5]
	v_pk_add_f32 v[2:3], v[6:7], v[2:3]
	v_pk_mul_f32 v[76:77], v[76:77], s[2:3] op_sel_hi:[1,0]
	v_pk_mul_f32 v[60:61], v[60:61], s[2:3] op_sel_hi:[1,0]
	v_pk_mul_f32 v[48:49], v[44:45], s[2:3] op_sel_hi:[1,0]
	v_pk_mul_f32 v[44:45], v[46:47], s[2:3] op_sel_hi:[1,0]
	v_lshl_add_u64 v[46:47], v[50:51], 0, s[28:29]
	v_cvt_pk_f16_f32 v18, v18, v19
	v_cvt_pk_f16_f32 v19, v20, v21
	v_pk_mul_f32 v[16:17], v[16:17], s[2:3] op_sel_hi:[1,0]
	v_cvt_pk_f16_f32 v20, v14, v15
	v_lshl_add_u64 v[14:15], v[30:31], 0, s[28:29]
	v_pk_mul_f32 v[12:13], v[12:13], s[2:3] op_sel_hi:[1,0]
	v_pk_mul_f32 v[10:11], v[10:11], s[2:3] op_sel_hi:[1,0]
	v_pk_mul_f32 v[4:5], v[4:5], s[2:3] op_sel_hi:[1,0]
	v_pk_mul_f32 v[2:3], v[2:3], s[2:3] op_sel_hi:[1,0]
	s_add_u32 s28, s20, s22
	v_cvt_pk_f16_f32 v81, v76, v77
	v_cvt_pk_f16_f32 v62, v62, v63
	v_cvt_pk_f16_f32 v63, v66, v67
	v_cvt_pk_f16_f32 v65, v60, v61
	v_cvt_pk_f16_f32 v42, v42, v43
	v_cvt_pk_f16_f32 v43, v52, v53
	v_cvt_pk_f16_f32 v44, v44, v45
	v_cvt_pk_f16_f32 v45, v48, v49
	v_cvt_pk_f16_f32 v21, v16, v17
	v_cvt_pk_f16_f32 v10, v10, v11
	v_cvt_pk_f16_f32 v11, v12, v13
	v_cvt_pk_f16_f32 v12, v2, v3
	v_cvt_pk_f16_f32 v13, v4, v5
	v_lshl_add_u64 v[2:3], v[30:31], 0, s[14:15]
	s_addc_u32 s29, s21, 0
	v_lshlrev_b32_e32 v92, 2, v1
	global_store_dwordx4 v[74:75], v[78:81], off sc1
	global_store_dwordx4 v[58:59], v[62:65], off sc1
	global_store_dwordx4 v[46:47], v[42:45], off sc1
	global_store_dwordx4 v[14:15], v[18:21], off sc1
	global_store_dwordx4 v[2:3], v[10:13], off sc1
	v_lshl_add_u64 v[2:3], s[28:29], 0, v[92:93]
	s_mov_b64 s[28:29], 0x1000
	v_lshl_add_u64 v[10:11], v[2:3], 0, s[28:29]
	global_load_dwordx4 v[22:25], v[10:11], off
	global_load_dwordx4 v[14:17], v[10:11], off offset:16
	global_load_dwordx4 v[6:9], v[10:11], off offset:512
	global_load_dwordx4 v[2:5], v[10:11], off offset:528
	s_mov_b32 s25, 1
	s_mov_b32 s26, 16
	s_mov_b32 s14, 2
	s_mov_b32 s15, 0x18000
	s_mov_b32 s2, 0xc000
	s_mov_b32 s27, 0
	v_mov_b32_e32 v10, v93
	v_mov_b32_e32 v11, v93
	v_mov_b32_e32 v12, v93
	v_mov_b32_e32 v13, v93
	v_mov_b32_e32 v18, v93
	v_mov_b32_e32 v19, v93
	v_mov_b32_e32 v20, v93
	v_mov_b32_e32 v21, v93
	v_mov_b32_e32 v26, v93
	v_mov_b32_e32 v27, v93
	v_mov_b32_e32 v28, v93
	v_mov_b32_e32 v29, v93
	v_mov_b32_e32 v34, v93
	v_mov_b32_e32 v35, v93
	v_mov_b32_e32 v36, v93
	v_mov_b32_e32 v37, v93
	v_mov_b32_e32 v42, v93
	v_mov_b32_e32 v43, v93
	v_mov_b32_e32 v44, v93
	v_mov_b32_e32 v45, v93
	v_mov_b32_e32 v50, v93
	v_mov_b32_e32 v51, v93
	v_mov_b32_e32 v52, v93
	v_mov_b32_e32 v53, v93
	v_mov_b32_e32 v62, v93
	v_mov_b32_e32 v63, v93
	v_mov_b32_e32 v64, v93
	v_mov_b32_e32 v65, v93
	v_mov_b32_e32 v70, v93
	v_mov_b32_e32 v71, v93
	v_mov_b32_e32 v72, v93
	v_mov_b32_e32 v73, v93
	v_mov_b32_e32 v30, v93
	v_mov_b32_e32 v31, v93
	v_mov_b32_e32 v32, v93
	v_mov_b32_e32 v33, v93
	v_mov_b32_e32 v38, v93
	v_mov_b32_e32 v39, v93
	v_mov_b32_e32 v40, v93
	v_mov_b32_e32 v41, v93
	v_mov_b32_e32 v46, v93
	v_mov_b32_e32 v47, v93
	v_mov_b32_e32 v48, v93
	v_mov_b32_e32 v49, v93
	v_mov_b32_e32 v54, v93
	v_mov_b32_e32 v55, v93
	v_mov_b32_e32 v56, v93
	v_mov_b32_e32 v57, v93
	v_mov_b32_e32 v58, v93
	v_mov_b32_e32 v59, v93
	v_mov_b32_e32 v60, v93
	v_mov_b32_e32 v61, v93
	v_mov_b32_e32 v66, v93
	v_mov_b32_e32 v67, v93
	v_mov_b32_e32 v68, v93
	v_mov_b32_e32 v69, v93
	v_mov_b32_e32 v74, v93
	v_mov_b32_e32 v75, v93
	v_mov_b32_e32 v76, v93
	v_mov_b32_e32 v77, v93
	v_mov_b32_e32 v78, v93
	v_mov_b32_e32 v79, v93
	v_mov_b32_e32 v80, v93
	v_mov_b32_e32 v81, v93
.LBB1_5:
	s_mov_b32 s28, s2
	v_add_u32_e32 v1, s28, v101
	ds_read_b128 v[106:109], v1 offset:16384
	ds_read_b128 v[110:113], v1 offset:17408
	ds_read_b128 v[114:117], v1 offset:18432
	ds_read_b128 v[118:121], v1 offset:19456
	ds_read_b128 v[122:125], v1 offset:32768
	ds_read_b128 v[126:129], v1 offset:33792
	ds_read_b128 v[130:133], v1 offset:34816
	ds_read_b128 v[134:137], v1 offset:35840
	v_add_u32_e32 v1, s28, v91
	ds_read_b128 v[138:141], v1
	ds_read_b128 v[142:145], v1 offset:1024
	ds_read_b128 v[146:149], v1 offset:2048
	ds_read_b128 v[150:153], v1 offset:3072
	ds_read_b128 v[154:157], v1 offset:4096
	ds_read_b128 v[158:161], v1 offset:5120
	ds_read_b128 v[162:165], v1 offset:6144
	ds_read_b128 v[166:169], v1 offset:7168
	s_lshl_b32 s2, s25, 2
	s_or_b32 s2, s2, s23
	s_lshl_b64 s[30:31], s[2:3], 19
	s_add_u32 s2, s6, s30
	s_addc_u32 s29, s7, s31
	s_lshl_b32 s33, s14, 7
	s_ashr_i32 s35, s33, 31
	s_add_u32 s30, s2, s33
	s_addc_u32 s31, s29, s35
	s_add_u32 s34, s4, s33
	s_addc_u32 s35, s5, s35
	s_add_i32 s2, s19, s27
	s_add_i32 m0, s2, 0x4000
	s_nop 0
	global_load_lds_dwordx4 v84, s[30:31]
	s_add_i32 m0, s2, 0x6000
	s_nop 0
	global_load_lds_dwordx4 v88, s[30:31]
	s_mov_b32 m0, s2
	s_nop 0
	global_load_lds_dwordx4 v82, s[34:35]
	s_waitcnt vmcnt(3)
	s_waitcnt lgkmcnt(0)
	s_barrier
	s_setprio 1
	s_waitcnt lgkmcnt(0)
	v_mfma_f32_16x16x32_f16 v[78:81], v[106:109], v[138:141], v[78:81]
	s_add_u32 s30, s30, 0x40000
	s_addc_u32 s31, s31, 0
	s_add_i32 m0, s2, 0x8000
	v_mfma_f32_16x16x32_f16 v[74:77], v[114:117], v[138:141], v[74:77]
	global_load_lds_dwordx4 v84, s[30:31]
	s_add_i32 m0, s2, 0xa000
	v_mfma_f32_16x16x32_f16 v[66:69], v[106:109], v[146:149], v[66:69]
	global_load_lds_dwordx4 v88, s[30:31]
	s_add_i32 m0, s2, 0x2000
	v_mfma_f32_16x16x32_f16 v[58:61], v[114:117], v[146:149], v[58:61]
	global_load_lds_dwordx4 v86, s[34:35]
	v_mfma_f32_16x16x32_f16 v[78:81], v[110:113], v[142:145], v[78:81]
	v_mfma_f32_16x16x32_f16 v[74:77], v[118:121], v[142:145], v[74:77]
	v_mfma_f32_16x16x32_f16 v[66:69], v[110:113], v[150:153], v[66:69]
	v_mfma_f32_16x16x32_f16 v[58:61], v[118:121], v[150:153], v[58:61]
	v_mfma_f32_16x16x32_f16 v[54:57], v[106:109], v[154:157], v[54:57]
	v_mfma_f32_16x16x32_f16 v[46:49], v[114:117], v[154:157], v[46:49]
	v_mfma_f32_16x16x32_f16 v[38:41], v[106:109], v[162:165], v[38:41]
	v_mfma_f32_16x16x32_f16 v[30:33], v[114:117], v[162:165], v[30:33]
	v_mfma_f32_16x16x32_f16 v[54:57], v[110:113], v[158:161], v[54:57]
	v_mfma_f32_16x16x32_f16 v[46:49], v[118:121], v[158:161], v[46:49]
	v_mfma_f32_16x16x32_f16 v[38:41], v[110:113], v[166:169], v[38:41]
	v_mfma_f32_16x16x32_f16 v[30:33], v[118:121], v[166:169], v[30:33]
	v_mfma_f32_16x16x32_f16 v[70:73], v[122:125], v[138:141], v[70:73]
	v_mfma_f32_16x16x32_f16 v[62:65], v[130:133], v[138:141], v[62:65]
	v_mfma_f32_16x16x32_f16 v[50:53], v[122:125], v[146:149], v[50:53]
	v_mfma_f32_16x16x32_f16 v[42:45], v[130:133], v[146:149], v[42:45]
	v_mfma_f32_16x16x32_f16 v[70:73], v[126:129], v[142:145], v[70:73]
	v_mfma_f32_16x16x32_f16 v[62:65], v[134:137], v[142:145], v[62:65]
	v_mfma_f32_16x16x32_f16 v[50:53], v[126:129], v[150:153], v[50:53]
	v_mfma_f32_16x16x32_f16 v[42:45], v[134:137], v[150:153], v[42:45]
	v_mfma_f32_16x16x32_f16 v[34:37], v[122:125], v[154:157], v[34:37]
	v_mfma_f32_16x16x32_f16 v[26:29], v[130:133], v[154:157], v[26:29]
	s_add_i32 s2, s14, 1
	s_cmp_lt_u32 s25, 2
	s_cselect_b64 s[30:31], -1, 0
	v_mfma_f32_16x16x32_f16 v[18:21], v[122:125], v[162:165], v[18:21]
	s_cmp_eq_u32 s2, 16
	s_cselect_b64 s[34:35], -1, 0
	v_mfma_f32_16x16x32_f16 v[10:13], v[130:133], v[162:165], v[10:13]
	s_and_b64 s[36:37], s[34:35], exec
	s_cselect_b32 s14, 0, s2
	v_mfma_f32_16x16x32_f16 v[34:37], v[126:129], v[158:161], v[34:37]
	s_and_b64 s[30:31], s[34:35], s[30:31]
	s_cmp_lg_u64 s[30:31], 0
	v_mfma_f32_16x16x32_f16 v[26:29], v[134:137], v[158:161], v[26:29]
	s_addc_u32 s25, s25, 0
	s_add_i32 s26, s26, -1
	v_mfma_f32_16x16x32_f16 v[18:21], v[126:129], v[166:169], v[18:21]
	s_mov_b32 s2, s15
	s_mov_b32 s15, s27
	v_mfma_f32_16x16x32_f16 v[10:13], v[134:137], v[166:169], v[10:13]
	s_mov_b32 s27, s28
	s_cmp_lg_u32 s26, 0
	s_setprio 0
	s_barrier
	s_cbranch_scc1 .LBB1_5
	s_ashr_i32 s2, s17, 7
	s_and_b32 s3, s2, -16
	s_or_b32 s2, s3, 2
	s_sub_u32 s14, s10, s8
	s_subb_u32 s11, s11, s9
	s_bfe_u32 s6, s17, 0x50006
	s_add_u32 s14, s8, s14
	s_addc_u32 s15, s9, s11
	s_lshr_b32 s11, s24, 6
	s_or_b32 s17, s11, s3
	s_lshl_b32 s17, s17, 8
	s_lshl_b32 s23, s6, 3
	v_bfe_u32 v93, v105, 3, 3
	v_pk_add_f32 v[80:81], v[24:25], v[80:81]
	v_pk_add_f32 v[78:79], v[22:23], v[78:79]
	v_pk_add_f32 v[74:75], v[14:15], v[74:75]
	s_or_b32 s17, s17, s23
	s_or_b32 s11, s2, s11
	v_cvt_pk_f16_f32 v78, v78, v79
	v_cvt_pk_f16_f32 v79, v80, v81
	v_cvt_pk_f16_f32 v80, v74, v75
	v_or_b32_e32 v74, s17, v93
	s_lshl_b32 s11, s11, 8
	v_ashrrev_i32_e32 v75, 31, v74
	v_pk_add_f32 v[72:73], v[8:9], v[72:73]
	v_pk_add_f32 v[70:71], v[6:7], v[70:71]
	v_pk_add_f32 v[62:63], v[2:3], v[62:63]
	s_or_b32 s11, s11, s23
	v_lshlrev_b64 v[74:75], 10, v[74:75]
	v_cvt_pk_f16_f32 v70, v70, v71
	v_cvt_pk_f16_f32 v71, v72, v73
	v_cvt_pk_f16_f32 v72, v62, v63
	v_or_b32_e32 v62, s11, v93
	v_pk_add_f32 v[76:77], v[16:17], v[76:77]
	v_lshl_add_u64 v[74:75], s[14:15], 0, v[74:75]
	v_ashrrev_i32_e32 v63, 31, v62
	v_cvt_pk_f16_f32 v81, v76, v77
	v_lshl_add_u64 v[76:77], v[74:75], 0, v[98:99]
	v_lshlrev_b64 v[62:63], 10, v[62:63]
	global_store_dwordx4 v[76:77], v[78:81], off sc1
	v_pk_add_f32 v[64:65], v[4:5], v[64:65]
	v_lshl_add_u64 v[76:77], s[14:15], 0, v[62:63]
	v_cvt_pk_f16_f32 v73, v64, v65
	v_lshl_add_u64 v[62:63], v[76:77], 0, v[98:99]
	global_store_dwordx4 v[62:63], v[70:73], off sc1
	v_pk_add_f32 v[64:65], v[24:25], v[68:69]
	v_pk_add_f32 v[62:63], v[22:23], v[66:67]
	v_pk_add_f32 v[60:61], v[16:17], v[60:61]
	v_pk_add_f32 v[58:59], v[14:15], v[58:59]
	v_pk_add_f32 v[52:53], v[8:9], v[52:53]
	v_pk_add_f32 v[50:51], v[6:7], v[50:51]
	v_pk_add_f32 v[44:45], v[4:5], v[44:45]
	v_pk_add_f32 v[42:43], v[2:3], v[42:43]
	v_cvt_pk_f16_f32 v62, v62, v63
	v_cvt_pk_f16_f32 v63, v64, v65
	v_cvt_pk_f16_f32 v64, v58, v59
	v_cvt_pk_f16_f32 v65, v60, v61
	v_lshl_add_u64 v[58:59], v[74:75], 0, v[96:97]
	v_cvt_pk_f16_f32 v50, v50, v51
	v_cvt_pk_f16_f32 v51, v52, v53
	v_cvt_pk_f16_f32 v52, v42, v43
	v_cvt_pk_f16_f32 v53, v44, v45
	v_lshl_add_u64 v[42:43], v[76:77], 0, v[96:97]
	v_mov_b32_e32 v1, 0
	global_store_dwordx4 v[58:59], v[62:65], off sc1
	global_store_dwordx4 v[42:43], v[50:53], off sc1
	v_pk_add_f32 v[44:45], v[24:25], v[56:57]
	v_pk_add_f32 v[42:43], v[22:23], v[54:55]
	v_mov_b32_e32 v95, v1
	v_cvt_pk_f16_f32 v42, v42, v43
	v_cvt_pk_f16_f32 v43, v44, v45
	v_pk_add_f32 v[48:49], v[16:17], v[48:49]
	v_pk_add_f32 v[44:45], v[14:15], v[46:47]
	v_pk_add_f32 v[36:37], v[8:9], v[36:37]
	v_pk_add_f32 v[34:35], v[6:7], v[34:35]
	v_pk_add_f32 v[28:29], v[4:5], v[28:29]
	v_pk_add_f32 v[26:27], v[2:3], v[26:27]
	v_pk_add_f32 v[24:25], v[24:25], v[40:41]
	v_pk_add_f32 v[22:23], v[22:23], v[38:39]
	v_pk_add_f32 v[16:17], v[16:17], v[32:33]
	v_pk_add_f32 v[14:15], v[14:15], v[30:31]
	v_pk_add_f32 v[8:9], v[8:9], v[20:21]
	v_pk_add_f32 v[6:7], v[6:7], v[18:19]
	v_pk_add_f32 v[4:5], v[4:5], v[12:13]
	v_pk_add_f32 v[2:3], v[2:3], v[10:11]
	s_add_u32 s14, s20, s22
	v_cvt_pk_f16_f32 v44, v44, v45
	v_cvt_pk_f16_f32 v45, v48, v49
	v_lshl_add_u64 v[46:47], v[74:75], 0, v[0:1]
	v_cvt_pk_f16_f32 v34, v34, v35
	v_cvt_pk_f16_f32 v35, v36, v37
	v_cvt_pk_f16_f32 v36, v26, v27
	v_cvt_pk_f16_f32 v37, v28, v29
	v_lshl_add_u64 v[26:27], v[76:77], 0, v[0:1]
	v_cvt_pk_f16_f32 v22, v22, v23
	v_cvt_pk_f16_f32 v23, v24, v25
	v_cvt_pk_f16_f32 v24, v14, v15
	v_cvt_pk_f16_f32 v25, v16, v17
	v_lshl_add_u64 v[14:15], v[74:75], 0, v[94:95]
	v_cvt_pk_f16_f32 v6, v6, v7
	v_cvt_pk_f16_f32 v7, v8, v9
	v_cvt_pk_f16_f32 v8, v2, v3
	v_cvt_pk_f16_f32 v9, v4, v5
	v_lshl_add_u64 v[2:3], v[76:77], 0, v[94:95]
	s_addc_u32 s15, s21, 0
	v_mov_b32_e32 v93, v1
	global_store_dwordx4 v[46:47], v[42:45], off sc1
	global_store_dwordx4 v[26:27], v[34:37], off sc1
	global_store_dwordx4 v[14:15], v[22:25], off sc1
	global_store_dwordx4 v[2:3], v[6:9], off sc1
	v_lshl_add_u64 v[2:3], s[14:15], 0, v[92:93]
	s_mov_b64 s[14:15], 0x2000
	v_lshl_add_u64 v[2:3], v[2:3], 0, s[14:15]
	global_load_dwordx4 v[20:23], v[2:3], off
	global_load_dwordx4 v[12:15], v[2:3], off offset:16
	global_load_dwordx4 v[8:11], v[2:3], off offset:512
	global_load_dwordx4 v[4:7], v[2:3], off offset:528
	s_add_u32 s11, s12, 0x400000
	s_mov_b32 s7, 2
	v_and_b32_e32 v106, 56, v105
	s_mov_b32 s10, 0
	s_addc_u32 s12, s13, 0
	s_mov_b32 s14, 0xc000
	s_mov_b32 s17, 0x18000
	s_mov_b32 s13, 16
	v_mov_b32_e32 v0, v1
	v_mov_b32_e32 v2, v1
	v_mov_b32_e32 v3, v1
	v_mov_b32_e32 v16, v1
	v_mov_b32_e32 v17, v1
	v_mov_b32_e32 v18, v1
	v_mov_b32_e32 v19, v1
	v_mov_b32_e32 v24, v1
	v_mov_b32_e32 v25, v1
	v_mov_b32_e32 v26, v1
	v_mov_b32_e32 v27, v1
	v_mov_b32_e32 v32, v1
	v_mov_b32_e32 v33, v1
	v_mov_b32_e32 v34, v1
	v_mov_b32_e32 v35, v1
	v_mov_b32_e32 v40, v1
	v_mov_b32_e32 v41, v1
	v_mov_b32_e32 v42, v1
	v_mov_b32_e32 v43, v1
	v_mov_b32_e32 v48, v1
	v_mov_b32_e32 v49, v1
	v_mov_b32_e32 v50, v1
	v_mov_b32_e32 v51, v1
	v_mov_b32_e32 v60, v1
	v_mov_b32_e32 v61, v1
	v_mov_b32_e32 v62, v1
	v_mov_b32_e32 v63, v1
	v_mov_b32_e32 v68, v1
	v_mov_b32_e32 v69, v1
	v_mov_b32_e32 v70, v1
	v_mov_b32_e32 v71, v1
	v_mov_b32_e32 v28, v1
	v_mov_b32_e32 v29, v1
	v_mov_b32_e32 v30, v1
	v_mov_b32_e32 v31, v1
	v_mov_b32_e32 v36, v1
	v_mov_b32_e32 v37, v1
	v_mov_b32_e32 v38, v1
	v_mov_b32_e32 v39, v1
	v_mov_b32_e32 v44, v1
	v_mov_b32_e32 v45, v1
	v_mov_b32_e32 v46, v1
	v_mov_b32_e32 v47, v1
	v_mov_b32_e32 v52, v1
	v_mov_b32_e32 v53, v1
	v_mov_b32_e32 v54, v1
	v_mov_b32_e32 v55, v1
	v_mov_b32_e32 v56, v1
	v_mov_b32_e32 v57, v1
	v_mov_b32_e32 v58, v1
	v_mov_b32_e32 v59, v1
	v_mov_b32_e32 v64, v1
	v_mov_b32_e32 v65, v1
	v_mov_b32_e32 v66, v1
	v_mov_b32_e32 v67, v1
	v_mov_b32_e32 v72, v1
	v_mov_b32_e32 v73, v1
	v_mov_b32_e32 v74, v1
	v_mov_b32_e32 v75, v1
	v_mov_b32_e32 v76, v1
	v_mov_b32_e32 v77, v1
	v_mov_b32_e32 v78, v1
	v_mov_b32_e32 v79, v1
.LBB1_7:
	s_mov_b32 s15, s17
	v_add_u32_e32 v80, s15, v101
	ds_read_b128 v[92:95], v80 offset:16384
	ds_read_b128 v[96:99], v80 offset:17408
	ds_read_b128 v[108:111], v80 offset:18432
	ds_read_b128 v[112:115], v80 offset:19456
	ds_read_b128 v[116:119], v80 offset:32768
	ds_read_b128 v[120:123], v80 offset:33792
	ds_read_b128 v[124:127], v80 offset:34816
	ds_read_b128 v[128:131], v80 offset:35840
	v_add_u32_e32 v80, s15, v91
	ds_read_b128 v[132:135], v80
	ds_read_b128 v[136:139], v80 offset:1024
	ds_read_b128 v[140:143], v80 offset:2048
	ds_read_b128 v[144:147], v80 offset:3072
	ds_read_b128 v[148:151], v80 offset:4096
	ds_read_b128 v[152:155], v80 offset:5120
	ds_read_b128 v[156:159], v80 offset:6144
	ds_read_b128 v[160:163], v80 offset:7168
	s_lshl_b32 s17, s7, 7
	s_ashr_i32 s23, s17, 31
	s_add_u32 s20, s11, s17
	s_addc_u32 s21, s12, s23
	s_add_u32 s22, s4, s17
	s_addc_u32 s23, s5, s23
	s_add_i32 s17, s19, s14
	s_add_i32 m0, s17, 0x4000
	s_nop 0
	global_load_lds_dwordx4 v84, s[20:21]
	s_add_i32 m0, s17, 0x6000
	s_nop 0
	global_load_lds_dwordx4 v88, s[20:21]
	s_mov_b32 m0, s17
	s_nop 0
	global_load_lds_dwordx4 v82, s[22:23]
	s_waitcnt vmcnt(3)
	s_waitcnt lgkmcnt(0)
	s_barrier
	s_setprio 1
	s_waitcnt lgkmcnt(0)
	v_mfma_f32_16x16x32_f16 v[76:79], v[92:95], v[132:135], v[76:79]
	s_add_u32 s20, s20, 0x40000
	s_addc_u32 s21, s21, 0
	s_add_i32 m0, s17, 0x8000
	v_mfma_f32_16x16x32_f16 v[72:75], v[108:111], v[132:135], v[72:75]
	global_load_lds_dwordx4 v84, s[20:21]
	s_add_i32 m0, s17, 0xa000
	v_mfma_f32_16x16x32_f16 v[64:67], v[92:95], v[140:143], v[64:67]
	global_load_lds_dwordx4 v88, s[20:21]
	s_add_i32 m0, s17, 0x2000
	v_mfma_f32_16x16x32_f16 v[56:59], v[108:111], v[140:143], v[56:59]
	global_load_lds_dwordx4 v86, s[22:23]
	v_mfma_f32_16x16x32_f16 v[76:79], v[96:99], v[136:139], v[76:79]
	v_mfma_f32_16x16x32_f16 v[72:75], v[112:115], v[136:139], v[72:75]
	v_mfma_f32_16x16x32_f16 v[64:67], v[96:99], v[144:147], v[64:67]
	v_mfma_f32_16x16x32_f16 v[56:59], v[112:115], v[144:147], v[56:59]
	v_mfma_f32_16x16x32_f16 v[52:55], v[92:95], v[148:151], v[52:55]
	v_mfma_f32_16x16x32_f16 v[44:47], v[108:111], v[148:151], v[44:47]
	v_mfma_f32_16x16x32_f16 v[36:39], v[92:95], v[156:159], v[36:39]
	v_mfma_f32_16x16x32_f16 v[28:31], v[108:111], v[156:159], v[28:31]
	v_mfma_f32_16x16x32_f16 v[52:55], v[96:99], v[152:155], v[52:55]
	v_mfma_f32_16x16x32_f16 v[44:47], v[112:115], v[152:155], v[44:47]
	v_mfma_f32_16x16x32_f16 v[36:39], v[96:99], v[160:163], v[36:39]
	v_mfma_f32_16x16x32_f16 v[28:31], v[112:115], v[160:163], v[28:31]
	v_mfma_f32_16x16x32_f16 v[68:71], v[116:119], v[132:135], v[68:71]
	v_mfma_f32_16x16x32_f16 v[60:63], v[124:127], v[132:135], v[60:63]
	v_mfma_f32_16x16x32_f16 v[48:51], v[116:119], v[140:143], v[48:51]
	v_mfma_f32_16x16x32_f16 v[40:43], v[124:127], v[140:143], v[40:43]
	v_mfma_f32_16x16x32_f16 v[68:71], v[120:123], v[136:139], v[68:71]
	v_mfma_f32_16x16x32_f16 v[60:63], v[128:131], v[136:139], v[60:63]
	v_mfma_f32_16x16x32_f16 v[48:51], v[120:123], v[144:147], v[48:51]
	v_mfma_f32_16x16x32_f16 v[40:43], v[128:131], v[144:147], v[40:43]
	v_mfma_f32_16x16x32_f16 v[32:35], v[116:119], v[148:151], v[32:35]
	v_mfma_f32_16x16x32_f16 v[24:27], v[124:127], v[148:151], v[24:27]
	s_add_i32 s7, s7, 1
	s_cmp_lg_u32 s7, 16
	v_mfma_f32_16x16x32_f16 v[16:19], v[116:119], v[156:159], v[16:19]
	s_cselect_b32 s7, s7, 0
	v_mfma_f32_16x16x32_f16 v[0:3], v[124:127], v[156:159], v[0:3]
	s_add_i32 s13, s13, -1
	v_mfma_f32_16x16x32_f16 v[32:35], v[120:123], v[152:155], v[32:35]
	s_mov_b32 s17, s10
	v_mfma_f32_16x16x32_f16 v[24:27], v[128:131], v[152:155], v[24:27]
	s_mov_b32 s10, s14
	v_mfma_f32_16x16x32_f16 v[16:19], v[120:123], v[160:163], v[16:19]
	s_mov_b32 s14, s15
	v_mfma_f32_16x16x32_f16 v[0:3], v[128:131], v[160:163], v[0:3]
	s_cmp_lg_u32 s13, 0
	s_setprio 0
	s_barrier
	s_cbranch_scc1 .LBB1_7
	s_sub_u32 s0, s0, s8
	s_subb_u32 s1, s1, s9
	s_add_u32 s0, s8, s0
	s_addc_u32 s1, s9, s1
	s_lshl_b32 s3, s3, 6
	s_or_b32 s3, s3, s16
	s_lshl_b32 s4, s6, 1
	v_lshrrev_b32_e32 v86, 5, v106
	v_pk_add_f32 v[78:79], v[22:23], v[78:79]
	v_pk_add_f32 v[76:77], v[20:21], v[76:77]
	v_pk_add_f32 v[72:73], v[12:13], v[72:73]
	s_or_b32 s3, s3, s4
	s_lshl_b32 s2, s2, 6
	v_cvt_pk_f16_f32 v76, v76, v77
	v_cvt_pk_f16_f32 v77, v78, v79
	v_cvt_pk_f16_f32 v78, v72, v73
	v_or_b32_e32 v72, s3, v86
	s_or_b32 s2, s2, s16
	v_ashrrev_i32_e32 v73, 31, v72
	v_pk_add_f32 v[70:71], v[10:11], v[70:71]
	v_pk_add_f32 v[68:69], v[8:9], v[68:69]
	v_pk_add_f32 v[60:61], v[4:5], v[60:61]
	s_or_b32 s2, s2, s4
	v_lshlrev_b64 v[72:73], 12, v[72:73]
	v_cvt_pk_f16_f32 v68, v68, v69
	v_cvt_pk_f16_f32 v69, v70, v71
	v_cvt_pk_f16_f32 v70, v60, v61
	v_or_b32_e32 v60, s2, v86
	v_mov_b32_e32 v91, 0
	v_pk_add_f32 v[74:75], v[14:15], v[74:75]
	v_lshl_add_u64 v[72:73], s[0:1], 0, v[72:73]
	v_ashrrev_i32_e32 v61, 31, v60
	v_cvt_pk_f16_f32 v79, v74, v75
	v_lshl_add_u64 v[74:75], v[72:73], 0, v[90:91]
	v_lshlrev_b64 v[60:61], 12, v[60:61]
	v_lshl_or_b32 v84, v102, 6, v100
	v_mov_b32_e32 v85, v91
	global_store_dwordx4 v[74:75], v[76:79], off sc1
	v_lshl_add_u64 v[74:75], s[0:1], 0, v[60:61]
	v_pk_add_f32 v[50:51], v[10:11], v[50:51]
	v_pk_add_f32 v[48:49], v[8:9], v[48:49]
	v_pk_add_f32 v[42:43], v[6:7], v[42:43]
	v_pk_add_f32 v[40:41], v[4:5], v[40:41]
	v_pk_add_f32 v[62:63], v[6:7], v[62:63]
	v_cvt_pk_f16_f32 v48, v48, v49
	v_cvt_pk_f16_f32 v49, v50, v51
	v_cvt_pk_f16_f32 v50, v40, v41
	v_cvt_pk_f16_f32 v51, v42, v43
	v_lshl_add_u64 v[40:41], v[74:75], 0, v[84:85]
	v_cvt_pk_f16_f32 v71, v62, v63
	v_lshl_add_u64 v[60:61], v[74:75], 0, v[90:91]
	global_store_dwordx4 v[40:41], v[48:51], off sc1
	v_pk_add_f32 v[42:43], v[22:23], v[54:55]
	v_pk_add_f32 v[40:41], v[20:21], v[52:53]
	v_lshl_or_b32 v80, v103, 6, v100
	v_lshl_or_b32 v82, v104, 6, v100
	v_mov_b32_e32 v81, v91
	v_mov_b32_e32 v83, v91
	global_store_dwordx4 v[60:61], v[68:71], off sc1
	v_pk_add_f32 v[62:63], v[22:23], v[66:67]
	v_pk_add_f32 v[60:61], v[20:21], v[64:65]
	v_pk_add_f32 v[58:59], v[14:15], v[58:59]
	v_pk_add_f32 v[56:57], v[12:13], v[56:57]
	v_cvt_pk_f16_f32 v40, v40, v41
	v_cvt_pk_f16_f32 v41, v42, v43
	v_pk_add_f32 v[46:47], v[14:15], v[46:47]
	v_pk_add_f32 v[42:43], v[12:13], v[44:45]
	v_pk_add_f32 v[34:35], v[10:11], v[34:35]
	v_pk_add_f32 v[32:33], v[8:9], v[32:33]
	v_pk_add_f32 v[26:27], v[6:7], v[26:27]
	v_pk_add_f32 v[24:25], v[4:5], v[24:25]
	v_pk_add_f32 v[22:23], v[22:23], v[38:39]
	v_pk_add_f32 v[20:21], v[20:21], v[36:37]
	v_pk_add_f32 v[14:15], v[14:15], v[30:31]
	v_pk_add_f32 v[12:13], v[12:13], v[28:29]
	v_pk_add_f32 v[10:11], v[10:11], v[18:19]
	v_pk_add_f32 v[8:9], v[8:9], v[16:17]
	v_pk_add_f32 v[2:3], v[6:7], v[2:3]
	v_pk_add_f32 v[0:1], v[4:5], v[0:1]
	v_cvt_pk_f16_f32 v60, v60, v61
	v_cvt_pk_f16_f32 v61, v62, v63
	v_cvt_pk_f16_f32 v62, v56, v57
	v_cvt_pk_f16_f32 v63, v58, v59
	v_lshl_add_u64 v[56:57], v[72:73], 0, v[84:85]
	v_cvt_pk_f16_f32 v42, v42, v43
	v_cvt_pk_f16_f32 v43, v46, v47
	v_lshl_add_u64 v[44:45], v[72:73], 0, v[80:81]
	v_cvt_pk_f16_f32 v32, v32, v33
	v_cvt_pk_f16_f32 v33, v34, v35
	v_cvt_pk_f16_f32 v34, v24, v25
	v_cvt_pk_f16_f32 v35, v26, v27
	v_lshl_add_u64 v[24:25], v[74:75], 0, v[80:81]
	v_cvt_pk_f16_f32 v20, v20, v21
	v_cvt_pk_f16_f32 v21, v22, v23
	v_cvt_pk_f16_f32 v22, v12, v13
	v_cvt_pk_f16_f32 v23, v14, v15
	v_lshl_add_u64 v[12:13], v[72:73], 0, v[82:83]
	v_cvt_pk_f16_f32 v8, v8, v9
	v_cvt_pk_f16_f32 v9, v10, v11
	v_cvt_pk_f16_f32 v10, v0, v1
	v_cvt_pk_f16_f32 v11, v2, v3
	v_lshl_add_u64 v[0:1], v[74:75], 0, v[82:83]
	global_store_dwordx4 v[56:57], v[60:63], off sc1
	global_store_dwordx4 v[44:45], v[40:43], off sc1
	global_store_dwordx4 v[24:25], v[32:35], off sc1
	global_store_dwordx4 v[12:13], v[20:23], off sc1
	global_store_dwordx4 v[0:1], v[8:11], off sc1
	s_waitcnt vmcnt(0)
	s_cmpk_gt_u32 s18, 0xff
	s_cbranch_scc1 .LBB1_10
	s_barrier

.LBB2_3:
	s_mov_b32 s16, s15
	v_add_u32_e32 v116, s16, v87
	v_add_u32_e32 v148, s16, v0
	ds_read_b128 v[88:91], v116 offset:16384
	ds_read_b128 v[92:95], v116 offset:17408
	ds_read_b128 v[96:99], v116 offset:18432
	ds_read_b128 v[100:103], v116 offset:19456
	ds_read_b128 v[104:107], v116 offset:32768
	ds_read_b128 v[108:111], v116 offset:33792
	ds_read_b128 v[112:115], v116 offset:34816
	ds_read_b128 v[116:119], v116 offset:35840
	ds_read_b128 v[120:123], v148
	ds_read_b128 v[124:127], v148 offset:1024
	ds_read_b128 v[128:131], v148 offset:2048
	ds_read_b128 v[132:135], v148 offset:3072
	ds_read_b128 v[136:139], v148 offset:4096
	ds_read_b128 v[140:143], v148 offset:5120
	ds_read_b128 v[144:147], v148 offset:6144
	ds_read_b128 v[148:151], v148 offset:7168
	s_lshl_b32 s15, s7, 7
	s_ashr_i32 s17, s15, 31
	s_add_u32 s18, s4, s15
	s_addc_u32 s19, s5, s17
	s_add_u32 s20, s2, s15
	s_addc_u32 s21, s3, s17
	s_add_i32 s15, s6, s14
	s_add_i32 m0, s15, 0x4000
	s_nop 0
	global_load_lds_dwordx4 v82, s[18:19]
	s_add_i32 m0, s15, 0x6000
	s_nop 0
	global_load_lds_dwordx4 v84, s[18:19]
	s_mov_b32 m0, s15
	s_nop 0
	global_load_lds_dwordx4 v82, s[20:21]
	s_waitcnt vmcnt(3)
	s_waitcnt lgkmcnt(0)
	s_barrier
	s_setprio 1
	s_waitcnt lgkmcnt(0)
	v_mfma_f32_16x16x32_f16 v[18:21], v[88:91], v[120:123], v[18:21]
	s_add_u32 s18, s18, 0x40000
	s_addc_u32 s19, s19, 0
	s_add_i32 m0, s15, 0x8000
	v_mfma_f32_16x16x32_f16 v[70:73], v[96:99], v[120:123], v[70:73]
	global_load_lds_dwordx4 v82, s[18:19]
	s_add_i32 m0, s15, 0xa000
	v_mfma_f32_16x16x32_f16 v[58:61], v[88:91], v[128:131], v[58:61]
	global_load_lds_dwordx4 v84, s[18:19]
	s_add_i32 m0, s15, 0x2000
	v_mfma_f32_16x16x32_f16 v[54:57], v[96:99], v[128:131], v[54:57]
	global_load_lds_dwordx4 v84, s[20:21]
	v_mfma_f32_16x16x32_f16 v[18:21], v[92:95], v[124:127], v[18:21]
	v_mfma_f32_16x16x32_f16 v[70:73], v[100:103], v[124:127], v[70:73]
	v_mfma_f32_16x16x32_f16 v[58:61], v[92:95], v[132:135], v[58:61]
	v_mfma_f32_16x16x32_f16 v[54:57], v[100:103], v[132:135], v[54:57]
	v_mfma_f32_16x16x32_f16 v[42:45], v[88:91], v[136:139], v[42:45]
	v_mfma_f32_16x16x32_f16 v[38:41], v[96:99], v[136:139], v[38:41]
	v_mfma_f32_16x16x32_f16 v[26:29], v[88:91], v[144:147], v[26:29]
	v_mfma_f32_16x16x32_f16 v[22:25], v[96:99], v[144:147], v[22:25]
	v_mfma_f32_16x16x32_f16 v[42:45], v[92:95], v[140:143], v[42:45]
	v_mfma_f32_16x16x32_f16 v[38:41], v[100:103], v[140:143], v[38:41]
	v_mfma_f32_16x16x32_f16 v[26:29], v[92:95], v[148:151], v[26:29]
	v_mfma_f32_16x16x32_f16 v[22:25], v[100:103], v[148:151], v[22:25]
	v_mfma_f32_16x16x32_f16 v[78:81], v[104:107], v[120:123], v[78:81]
	v_mfma_f32_16x16x32_f16 v[74:77], v[112:115], v[120:123], v[74:77]
	v_mfma_f32_16x16x32_f16 v[66:69], v[104:107], v[128:131], v[66:69]
	v_mfma_f32_16x16x32_f16 v[62:65], v[112:115], v[128:131], v[62:65]
	v_mfma_f32_16x16x32_f16 v[78:81], v[108:111], v[124:127], v[78:81]
	v_mfma_f32_16x16x32_f16 v[74:77], v[116:119], v[124:127], v[74:77]
	v_mfma_f32_16x16x32_f16 v[66:69], v[108:111], v[132:135], v[66:69]
	v_mfma_f32_16x16x32_f16 v[62:65], v[116:119], v[132:135], v[62:65]
	v_mfma_f32_16x16x32_f16 v[50:53], v[104:107], v[136:139], v[50:53]
	v_mfma_f32_16x16x32_f16 v[46:49], v[112:115], v[136:139], v[46:49]
	s_add_i32 s7, s7, 1
	s_cmp_lg_u32 s7, 16
	v_mfma_f32_16x16x32_f16 v[34:37], v[104:107], v[144:147], v[34:37]
	s_cselect_b32 s7, s7, 0
	v_mfma_f32_16x16x32_f16 v[30:33], v[112:115], v[144:147], v[30:33]
	s_add_i32 s11, s11, -1
	v_mfma_f32_16x16x32_f16 v[50:53], v[108:111], v[140:143], v[50:53]
	s_mov_b32 s15, s13
	v_mfma_f32_16x16x32_f16 v[46:49], v[116:119], v[140:143], v[46:49]
	s_mov_b32 s13, s14
	v_mfma_f32_16x16x32_f16 v[34:37], v[108:111], v[148:151], v[34:37]
	s_mov_b32 s14, s16
	v_mfma_f32_16x16x32_f16 v[30:33], v[116:119], v[148:151], v[30:33]
	s_cmp_lg_u32 s11, 0
	s_setprio 0
	s_barrier
	s_cbranch_scc1 .LBB2_3
	v_lshl_add_u32 v0, s0, 7, v86
	v_or_b32_e32 v88, s10, v1
	v_ashrrev_i32_e32 v1, 31, v0
	v_lshlrev_b64 v[82:83], 12, v[0:1]
	v_or_b32_e32 v88, s1, v88
	v_lshl_add_u64 v[82:83], s[8:9], 0, v[82:83]
	v_lshlrev_b32_e32 v88, 2, v88
	v_mov_b32_e32 v89, 0
	v_or_b32_e32 v84, 16, v0
	v_lshl_add_u64 v[82:83], v[82:83], 0, v[88:89]
	v_pk_add_f32 v[20:21], v[16:17], v[20:21]
	v_pk_add_f32 v[18:19], v[14:15], v[18:19]
	v_ashrrev_i32_e32 v85, 31, v84
	global_store_dwordx4 v[82:83], v[18:21], off sc1
	v_lshlrev_b64 v[84:85], 12, v[84:85]
	v_lshl_add_u64 v[84:85], s[8:9], 0, v[84:85]
	v_pk_add_f32 v[20:21], v[12:13], v[72:73]
	v_pk_add_f32 v[18:19], v[10:11], v[70:71]
	global_store_dwordx4 v[82:83], v[18:21], off offset:64 sc1
	v_or_b32_e32 v86, 32, v0
	v_lshl_add_u64 v[84:85], v[84:85], 0, v[88:89]
	v_pk_add_f32 v[20:21], v[8:9], v[80:81]
	v_pk_add_f32 v[18:19], v[6:7], v[78:79]
	global_store_dwordx4 v[82:83], v[18:21], off offset:512 sc1
	v_ashrrev_i32_e32 v87, 31, v86
	v_lshlrev_b64 v[86:87], 12, v[86:87]
	v_pk_add_f32 v[20:21], v[4:5], v[76:77]
	v_pk_add_f32 v[18:19], v[2:3], v[74:75]
	global_store_dwordx4 v[82:83], v[18:21], off offset:576 sc1
	v_lshl_add_u64 v[86:87], s[8:9], 0, v[86:87]
	v_or_b32_e32 v0, 48, v0
	v_pk_add_f32 v[20:21], v[16:17], v[60:61]
	v_pk_add_f32 v[18:19], v[14:15], v[58:59]
	global_store_dwordx4 v[84:85], v[18:21], off sc1
	v_ashrrev_i32_e32 v1, 31, v0
	v_lshl_add_u64 v[86:87], v[86:87], 0, v[88:89]
	v_pk_add_f32 v[20:21], v[12:13], v[56:57]
	v_pk_add_f32 v[18:19], v[10:11], v[54:55]
	global_store_dwordx4 v[84:85], v[18:21], off offset:64 sc1
	v_lshlrev_b64 v[0:1], 12, v[0:1]
	v_lshl_add_u64 v[0:1], s[8:9], 0, v[0:1]
	v_pk_add_f32 v[20:21], v[8:9], v[68:69]
	v_pk_add_f32 v[18:19], v[6:7], v[66:67]
	global_store_dwordx4 v[84:85], v[18:21], off offset:512 sc1
	v_lshl_add_u64 v[0:1], v[0:1], 0, v[88:89]
	s_cmpk_gt_u32 s12, 0xff
	v_pk_add_f32 v[20:21], v[4:5], v[64:65]
	v_pk_add_f32 v[18:19], v[2:3], v[62:63]
	global_store_dwordx4 v[84:85], v[18:21], off offset:576 sc1
	s_nop 1
	v_pk_add_f32 v[20:21], v[16:17], v[44:45]
	v_pk_add_f32 v[18:19], v[14:15], v[42:43]
	global_store_dwordx4 v[86:87], v[18:21], off sc1
	v_pk_add_f32 v[16:17], v[16:17], v[28:29]
	v_pk_add_f32 v[14:15], v[14:15], v[26:27]
	v_pk_add_f32 v[20:21], v[12:13], v[40:41]
	v_pk_add_f32 v[18:19], v[10:11], v[38:39]
	global_store_dwordx4 v[86:87], v[18:21], off offset:64 sc1
	v_pk_add_f32 v[12:13], v[12:13], v[24:25]
	v_pk_add_f32 v[10:11], v[10:11], v[22:23]
	v_pk_add_f32 v[20:21], v[8:9], v[52:53]
	v_pk_add_f32 v[18:19], v[6:7], v[50:51]
	global_store_dwordx4 v[86:87], v[18:21], off offset:512 sc1
	v_pk_add_f32 v[8:9], v[8:9], v[36:37]
	v_pk_add_f32 v[6:7], v[6:7], v[34:35]
	v_pk_add_f32 v[20:21], v[4:5], v[48:49]
	v_pk_add_f32 v[18:19], v[2:3], v[46:47]
	v_pk_add_f32 v[4:5], v[4:5], v[32:33]
	v_pk_add_f32 v[2:3], v[2:3], v[30:31]
	global_store_dwordx4 v[86:87], v[18:21], off offset:576 sc1
	global_store_dwordx4 v[0:1], v[14:17], off sc1
	global_store_dwordx4 v[0:1], v[10:13], off offset:64 sc1
	global_store_dwordx4 v[0:1], v[6:9], off offset:512 sc1
	global_store_dwordx4 v[0:1], v[2:5], off offset:576 sc1
	s_waitcnt vmcnt(0)
	s_cbranch_scc1 .LBB2_6
	s_barrier
